# out-proj L1 epilogue: all 15 residual-row loads issued at the top (one wait)
# speedup vs baseline: 1.0080x; 1.0080x over previous
;     __device__ __forceinline__ void operator()() { if (cnt == turn) run_all(tid_); ++cnt; }
;     __device__ __forceinline__ void operator()(const Acc& acc, const Unit& u, int wr, int wc, int fr, int fq) const {
;         const int col0 = u.pn * BM + wc * 32 + 8 * fq; const int b = (u.pm * BM) / SEQ;
;         f32x4 gv[2][2];
; #pragma unroll
;         for (int bj = 0; bj < 2; ++bj)
; #pragma unroll
;             for (int n = 0; n < 2; ++n) gv[bj][n] = *(const f32x4*)(gate + (size_t)b * gstride + col0 + bj * HALF + 4 * n);
; #pragma unroll
;         for (int ai = 0; ai < 2; ++ai)
; #pragma unroll
;             for (int m = 0; m < 4; ++m) { const size_t off = (size_t)(u.pm * BM + ai * HALF + wr * 64 + m * 16 + fr) * DM + col0;
; #pragma unroll
;                 for (int bj = 0; bj < 2; ++bj) { f32x4 b0, b1;
;                     if constexpr (BASE16) { const f16x8 bv = *(const f16x8*)((const f16*)base + off + bj * HALF);
;                         b0 = (f32x4){(float)bv[0], (float)bv[1], (float)bv[2], (float)bv[3]}; b1 = (f32x4){(float)bv[4], (float)bv[5], (float)bv[6], (float)bv[7]}; }
;                     else { b0 = *(const f32x4*)((const float*)base + off + bj * HALF); b1 = *(const f32x4*)((const float*)base + off + bj * HALF + 4); }
;                     const f32x4 v0 = b0 + gv[bj][0] * acc[ai][bj][m][0], v1 = b1 + gv[bj][1] * acc[ai][bj][m][1];
;                     u32x4 w; w.x = pkh(v0[0], v0[1]); w.y = pkh(v0[2], v0[3]); w.z = pkh(v1[0], v1[1]); w.w = pkh(v1[2], v1[3]);
;                     *(u32x4*)(out + off + bj * HALF) = w; }
;                 if (m & 1) asm volatile("" ::: "memory"); }
.LBB0_1483:
	v_lshl_add_u32 v164, s2, 8, v1
	v_lshl_or_b32 v162, s3, 8, v167
	v_ashrrev_i32_e32 v165, 31, v164
	s_ashr_i32 s3, s2, 31
	v_ashrrev_i32_e32 v163, 31, v162
	v_lshlrev_b64 v[122:123], 10, v[164:165]
	s_lshr_b32 s3, s3, 29
	v_lshl_add_u64 v[122:123], v[122:123], 0, v[162:163]
	v_lshlrev_b64 v[130:131], 1, v[122:123]
	s_add_i32 s2, s2, s3
	v_lshl_add_u64 v[176:177], s[66:67], 0, v[130:131]
	s_ashr_i32 s2, s2, 3
	global_load_dwordx4 v[172:175], v[176:177], off
	s_mul_hi_i32 s3, s2, 0x6000
	s_mulk_i32 s2, 0x6000
	s_add_u32 s2, s38, s2
	s_addc_u32 s3, s39, s3
	v_lshl_add_u64 v[134:135], v[162:163], 2, s[2:3]
	global_load_dwordx4 v[126:129], v[134:135], off
	global_load_dwordx4 v[122:125], v[134:135], off offset:16
	v_lshl_add_u64 v[178:179], s[8:9], 0, v[130:131]
	global_load_dwordx4 v[130:133], v[134:135], off offset:528
	s_nop 0
	global_load_dwordx4 v[134:137], v[134:135], off offset:512
	v_subrev_u32_e32 v246, s66, v176
	v_mov_b32_e32 v247, v246
	global_load_dwordx4 v[186:189], v247, s[66:67] offset:256
	v_add_u32_e32 v247, 0x8000, v246
	global_load_dwordx4 v[190:193], v247, s[66:67]
	v_add_u32_e32 v247, 0x8000, v246
	global_load_dwordx4 v[194:197], v247, s[66:67] offset:256
	v_add_u32_e32 v247, 0x10000, v246
	global_load_dwordx4 v[198:201], v247, s[66:67]
	v_add_u32_e32 v247, 0x10000, v246
	global_load_dwordx4 v[202:205], v247, s[66:67] offset:256
	v_add_u32_e32 v247, 0x18000, v246
	global_load_dwordx4 v[206:209], v247, s[66:67]
	v_add_u32_e32 v247, 0x18000, v246
	global_load_dwordx4 v[210:213], v247, s[66:67] offset:256
	v_add_u32_e32 v247, 0x40000, v246
	global_load_dwordx4 v[214:217], v247, s[66:67]
	v_add_u32_e32 v247, 0x40000, v246
	global_load_dwordx4 v[218:221], v247, s[66:67] offset:256
	v_add_u32_e32 v247, 0x48000, v246
	global_load_dwordx4 v[222:225], v247, s[66:67]
	v_add_u32_e32 v247, 0x48000, v246
	global_load_dwordx4 v[226:229], v247, s[66:67] offset:256
	v_add_u32_e32 v247, 0x50000, v246
	global_load_dwordx4 v[230:233], v247, s[66:67]
	v_add_u32_e32 v247, 0x50000, v246
	global_load_dwordx4 v[234:237], v247, s[66:67] offset:256
	v_add_u32_e32 v247, 0x58000, v246
	global_load_dwordx4 v[238:241], v247, s[66:67]
	v_add_u32_e32 v247, 0x58000, v246
	global_load_dwordx4 v[242:245], v247, s[66:67] offset:256
	s_andn2_b64 vcc, exec, s[4:5]
	s_mov_b64 s[2:3], -1
	s_waitcnt vmcnt(0)
	v_cvt_f32_f16_e32 v180, v172
	v_cvt_f32_f16_sdwa v181, v172 dst_sel:DWORD dst_unused:UNUSED_PAD src0_sel:WORD_1
	v_cvt_f32_f16_e32 v172, v173
	v_cvt_f32_f16_sdwa v173, v173 dst_sel:DWORD dst_unused:UNUSED_PAD src0_sel:WORD_1
	v_cvt_f32_f16_e32 v182, v174
	v_cvt_f32_f16_e32 v184, v175
	v_cvt_f32_f16_sdwa v185, v175 dst_sel:DWORD dst_unused:UNUSED_PAD src0_sel:WORD_1
	v_cvt_f32_f16_sdwa v183, v174 dst_sel:DWORD dst_unused:UNUSED_PAD src0_sel:WORD_1
	v_pk_fma_f32 v[144:145], v[144:145], v[128:129], v[172:173]
	v_pk_fma_f32 v[142:143], v[142:143], v[126:127], v[180:181]
	v_pk_fma_f32 v[172:173], v[140:141], v[124:125], v[184:185]
	v_pk_fma_f32 v[140:141], v[138:139], v[122:123], v[182:183]
	v_cvt_pk_f16_f32 v138, v142, v143
	v_cvt_pk_f16_f32 v139, v144, v145
	v_cvt_pk_f16_f32 v140, v140, v141
	v_cvt_pk_f16_f32 v141, v172, v173
	global_store_dwordx4 v[178:179], v[138:141], off
	s_nop 0
	v_or_b32_e32 v142, 16, v164
	v_ashrrev_i32_e32 v143, 31, v142
	v_lshlrev_b64 v[142:143], 10, v[142:143]
	v_lshl_add_u64 v[142:143], v[142:143], 0, v[162:163]
	v_lshlrev_b64 v[142:143], 1, v[142:143]
	v_lshl_add_u64 v[144:145], s[66:67], 0, v[142:143]
	s_nop 0
	v_mov_b32_e32 v138, v186
	v_mov_b32_e32 v139, v187
	v_mov_b32_e32 v140, v188
	v_mov_b32_e32 v141, v189
	v_cvt_f32_f16_e32 v172, v138
	v_cvt_f32_f16_sdwa v173, v138 dst_sel:DWORD dst_unused:UNUSED_PAD src0_sel:WORD_1
	v_cvt_f32_f16_e32 v138, v139
	v_cvt_f32_f16_sdwa v139, v139 dst_sel:DWORD dst_unused:UNUSED_PAD src0_sel:WORD_1
	v_cvt_f32_f16_e32 v174, v140
	v_cvt_f32_f16_e32 v176, v141
	v_cvt_f32_f16_sdwa v177, v141 dst_sel:DWORD dst_unused:UNUSED_PAD src0_sel:WORD_1
	v_cvt_f32_f16_sdwa v175, v140 dst_sel:DWORD dst_unused:UNUSED_PAD src0_sel:WORD_1
	v_pk_fma_f32 v[120:121], v[120:121], v[136:137], v[138:139]
	v_pk_fma_f32 v[118:119], v[118:119], v[134:135], v[172:173]
	v_pk_fma_f32 v[138:139], v[116:117], v[132:133], v[176:177]
	v_pk_fma_f32 v[116:117], v[114:115], v[130:131], v[174:175]
	v_cvt_pk_f16_f32 v114, v118, v119
	v_cvt_pk_f16_f32 v115, v120, v121
	v_cvt_pk_f16_f32 v116, v116, v117
	v_cvt_pk_f16_f32 v117, v138, v139
	global_store_dwordx4 v[178:179], v[114:117], off offset:256
	s_nop 0
	v_lshl_add_u64 v[118:119], s[8:9], 0, v[142:143]
	s_nop 0
	v_mov_b32_e32 v114, v190
	v_mov_b32_e32 v115, v191
	v_mov_b32_e32 v116, v192
	v_mov_b32_e32 v117, v193
	v_cvt_f32_f16_e32 v120, v114
	v_cvt_f32_f16_sdwa v121, v114 dst_sel:DWORD dst_unused:UNUSED_PAD src0_sel:WORD_1
	v_cvt_f32_f16_e32 v114, v115
	v_cvt_f32_f16_sdwa v115, v115 dst_sel:DWORD dst_unused:UNUSED_PAD src0_sel:WORD_1
	v_cvt_f32_f16_e32 v138, v116
	v_cvt_f32_f16_e32 v140, v117
	v_cvt_f32_f16_sdwa v141, v117 dst_sel:DWORD dst_unused:UNUSED_PAD src0_sel:WORD_1
	v_cvt_f32_f16_sdwa v139, v116 dst_sel:DWORD dst_unused:UNUSED_PAD src0_sel:WORD_1
	v_pk_fma_f32 v[112:113], v[112:113], v[128:129], v[114:115]
	v_pk_fma_f32 v[110:111], v[110:111], v[126:127], v[120:121]
	v_pk_fma_f32 v[114:115], v[108:109], v[124:125], v[140:141]
	v_pk_fma_f32 v[108:109], v[106:107], v[122:123], v[138:139]
	v_cvt_pk_f16_f32 v106, v110, v111
	v_cvt_pk_f16_f32 v107, v112, v113
	v_cvt_pk_f16_f32 v108, v108, v109
	v_cvt_pk_f16_f32 v109, v114, v115
	global_store_dwordx4 v[118:119], v[106:109], off
	s_nop 0
	v_or_b32_e32 v110, 32, v164
	v_ashrrev_i32_e32 v111, 31, v110
;     __device__ __forceinline__ void operator()(const Acc& acc, const Unit& u, int wr, int wc, int fr, int fq) const {
;     ...
;         for (int ai = 0; ai < 2; ++ai)
; #pragma unroll
;             for (int m = 0; m < 4; ++m) { const size_t off = (size_t)(u.pm * BM + ai * HALF + wr * 64 + m * 16 + fr) * DM + col0;
; #pragma unroll
;                 for (int bj = 0; bj < 2; ++bj) { f32x4 b0, b1;
;                     if constexpr (BASE16) { const f16x8 bv = *(const f16x8*)((const f16*)base + off + bj * HALF);
;                         b0 = (f32x4){(float)bv[0], (float)bv[1], (float)bv[2], (float)bv[3]}; b1 = (f32x4){(float)bv[4], (float)bv[5], (float)bv[6], (float)bv[7]}; }
;                     else { b0 = *(const f32x4*)((const float*)base + off + bj * HALF); b1 = *(const f32x4*)((const float*)base + off + bj * HALF + 4); }
;                     const f32x4 v0 = b0 + gv[bj][0] * acc[ai][bj][m][0], v1 = b1 + gv[bj][1] * acc[ai][bj][m][1];
;                     u32x4 w; w.x = pkh(v0[0], v0[1]); w.y = pkh(v0[2], v0[3]); w.z = pkh(v1[0], v1[1]); w.w = pkh(v1[2], v1[3]);
;                     *(u32x4*)(out + off + bj * HALF) = w; }
;                 if (m & 1) asm volatile("" ::: "memory"); }
	v_lshlrev_b64 v[110:111], 10, v[110:111]
	v_lshl_add_u64 v[110:111], v[110:111], 0, v[162:163]
	v_lshlrev_b64 v[110:111], 1, v[110:111]
	v_lshl_add_u64 v[112:113], s[66:67], 0, v[110:111]
	s_nop 0
	v_mov_b32_e32 v106, v194
	v_mov_b32_e32 v107, v195
	v_mov_b32_e32 v108, v196
	v_mov_b32_e32 v109, v197
	v_cvt_f32_f16_e32 v114, v106
	v_cvt_f32_f16_sdwa v115, v106 dst_sel:DWORD dst_unused:UNUSED_PAD src0_sel:WORD_1
	v_cvt_f32_f16_e32 v106, v107
	v_cvt_f32_f16_sdwa v107, v107 dst_sel:DWORD dst_unused:UNUSED_PAD src0_sel:WORD_1
	v_cvt_f32_f16_e32 v116, v108
	v_cvt_f32_f16_e32 v120, v109
	v_cvt_f32_f16_sdwa v121, v109 dst_sel:DWORD dst_unused:UNUSED_PAD src0_sel:WORD_1
	v_cvt_f32_f16_sdwa v117, v108 dst_sel:DWORD dst_unused:UNUSED_PAD src0_sel:WORD_1
	v_pk_fma_f32 v[104:105], v[104:105], v[136:137], v[106:107]
	v_pk_fma_f32 v[102:103], v[102:103], v[134:135], v[114:115]
	v_pk_fma_f32 v[106:107], v[100:101], v[132:133], v[120:121]
	v_pk_fma_f32 v[100:101], v[98:99], v[130:131], v[116:117]
	v_cvt_pk_f16_f32 v98, v102, v103
	v_cvt_pk_f16_f32 v99, v104, v105
	v_cvt_pk_f16_f32 v100, v100, v101
	v_cvt_pk_f16_f32 v101, v106, v107
	global_store_dwordx4 v[118:119], v[98:101], off offset:256
	s_nop 0
	v_lshl_add_u64 v[102:103], s[8:9], 0, v[110:111]
	s_nop 0
	v_mov_b32_e32 v98, v198
	v_mov_b32_e32 v99, v199
	v_mov_b32_e32 v100, v200
	v_mov_b32_e32 v101, v201
	v_cvt_f32_f16_e32 v104, v98
	v_cvt_f32_f16_sdwa v105, v98 dst_sel:DWORD dst_unused:UNUSED_PAD src0_sel:WORD_1
	v_cvt_f32_f16_e32 v98, v99
	v_cvt_f32_f16_sdwa v99, v99 dst_sel:DWORD dst_unused:UNUSED_PAD src0_sel:WORD_1
	v_cvt_f32_f16_e32 v106, v100
	v_cvt_f32_f16_e32 v108, v101
	v_cvt_f32_f16_sdwa v109, v101 dst_sel:DWORD dst_unused:UNUSED_PAD src0_sel:WORD_1
	v_cvt_f32_f16_sdwa v107, v100 dst_sel:DWORD dst_unused:UNUSED_PAD src0_sel:WORD_1
	v_pk_fma_f32 v[96:97], v[96:97], v[128:129], v[98:99]
	v_pk_fma_f32 v[94:95], v[94:95], v[126:127], v[104:105]
	v_pk_fma_f32 v[98:99], v[92:93], v[124:125], v[108:109]
	v_pk_fma_f32 v[92:93], v[90:91], v[122:123], v[106:107]
	v_cvt_pk_f16_f32 v90, v94, v95
	v_cvt_pk_f16_f32 v91, v96, v97
	v_cvt_pk_f16_f32 v92, v92, v93
	v_cvt_pk_f16_f32 v93, v98, v99
	global_store_dwordx4 v[102:103], v[90:93], off
	s_nop 0
	v_or_b32_e32 v94, 48, v164
	v_ashrrev_i32_e32 v95, 31, v94
	v_lshlrev_b64 v[94:95], 10, v[94:95]
	v_lshl_add_u64 v[94:95], v[94:95], 0, v[162:163]
	v_lshlrev_b64 v[94:95], 1, v[94:95]
	v_lshl_add_u64 v[96:97], s[66:67], 0, v[94:95]
	s_nop 0
	v_mov_b32_e32 v90, v202
	v_mov_b32_e32 v91, v203
	v_mov_b32_e32 v92, v204
	v_mov_b32_e32 v93, v205
	v_cvt_f32_f16_e32 v98, v90
	v_cvt_f32_f16_sdwa v99, v90 dst_sel:DWORD dst_unused:UNUSED_PAD src0_sel:WORD_1
	v_cvt_f32_f16_e32 v90, v91
	v_cvt_f32_f16_sdwa v91, v91 dst_sel:DWORD dst_unused:UNUSED_PAD src0_sel:WORD_1
	v_cvt_f32_f16_e32 v100, v92
	v_cvt_f32_f16_e32 v104, v93
	v_cvt_f32_f16_sdwa v105, v93 dst_sel:DWORD dst_unused:UNUSED_PAD src0_sel:WORD_1
	v_cvt_f32_f16_sdwa v101, v92 dst_sel:DWORD dst_unused:UNUSED_PAD src0_sel:WORD_1
	v_pk_fma_f32 v[88:89], v[88:89], v[136:137], v[90:91]
	v_pk_fma_f32 v[86:87], v[86:87], v[134:135], v[98:99]
	v_pk_fma_f32 v[90:91], v[84:85], v[132:133], v[104:105]
	v_pk_fma_f32 v[84:85], v[82:83], v[130:131], v[100:101]
	v_cvt_pk_f16_f32 v82, v86, v87
	v_cvt_pk_f16_f32 v83, v88, v89
	v_cvt_pk_f16_f32 v84, v84, v85
	v_cvt_pk_f16_f32 v85, v90, v91
	global_store_dwordx4 v[102:103], v[82:85], off offset:256
	s_nop 0
	v_lshl_add_u64 v[86:87], s[8:9], 0, v[94:95]
	s_nop 0
	v_mov_b32_e32 v82, v206
	v_mov_b32_e32 v83, v207
	v_mov_b32_e32 v84, v208
	v_mov_b32_e32 v85, v209
	v_cvt_f32_f16_e32 v88, v82
	v_cvt_f32_f16_sdwa v89, v82 dst_sel:DWORD dst_unused:UNUSED_PAD src0_sel:WORD_1
	v_cvt_f32_f16_e32 v82, v83
	v_cvt_f32_f16_sdwa v83, v83 dst_sel:DWORD dst_unused:UNUSED_PAD src0_sel:WORD_1
	v_cvt_f32_f16_e32 v90, v84
	v_cvt_f32_f16_e32 v92, v85
	v_cvt_f32_f16_sdwa v93, v85 dst_sel:DWORD dst_unused:UNUSED_PAD src0_sel:WORD_1
	v_cvt_f32_f16_sdwa v91, v84 dst_sel:DWORD dst_unused:UNUSED_PAD src0_sel:WORD_1
	v_pk_fma_f32 v[80:81], v[80:81], v[128:129], v[82:83]
	v_pk_fma_f32 v[78:79], v[78:79], v[126:127], v[88:89]
	v_pk_fma_f32 v[82:83], v[76:77], v[124:125], v[92:93]
	v_pk_fma_f32 v[76:77], v[74:75], v[122:123], v[90:91]
	v_cvt_pk_f16_f32 v74, v78, v79
	v_cvt_pk_f16_f32 v75, v80, v81
	v_cvt_pk_f16_f32 v76, v76, v77
	v_cvt_pk_f16_f32 v77, v82, v83
	global_store_dwordx4 v[86:87], v[74:77], off
	s_nop 0
	v_add_u32_e32 v78, 0x80, v164
	v_ashrrev_i32_e32 v79, 31, v78
	v_lshlrev_b64 v[78:79], 10, v[78:79]
	v_lshl_add_u64 v[78:79], v[78:79], 0, v[162:163]
	v_lshlrev_b64 v[78:79], 1, v[78:79]
	v_lshl_add_u64 v[80:81], s[66:67], 0, v[78:79]
	s_nop 0
	v_mov_b32_e32 v74, v210
	v_mov_b32_e32 v75, v211
	v_mov_b32_e32 v76, v212
	v_mov_b32_e32 v77, v213
	v_cvt_f32_f16_e32 v82, v74
	v_cvt_f32_f16_sdwa v83, v74 dst_sel:DWORD dst_unused:UNUSED_PAD src0_sel:WORD_1
	v_cvt_f32_f16_e32 v74, v75
	v_cvt_f32_f16_sdwa v75, v75 dst_sel:DWORD dst_unused:UNUSED_PAD src0_sel:WORD_1
	v_cvt_f32_f16_e32 v84, v76
	v_cvt_f32_f16_e32 v88, v77
	v_cvt_f32_f16_sdwa v89, v77 dst_sel:DWORD dst_unused:UNUSED_PAD src0_sel:WORD_1
	v_cvt_f32_f16_sdwa v85, v76 dst_sel:DWORD dst_unused:UNUSED_PAD src0_sel:WORD_1
	v_pk_fma_f32 v[72:73], v[72:73], v[136:137], v[74:75]
	v_pk_fma_f32 v[70:71], v[70:71], v[134:135], v[82:83]
	v_pk_fma_f32 v[74:75], v[68:69], v[132:133], v[88:89]
	v_pk_fma_f32 v[68:69], v[66:67], v[130:131], v[84:85]
	v_cvt_pk_f16_f32 v66, v70, v71
	v_cvt_pk_f16_f32 v67, v72, v73
	v_cvt_pk_f16_f32 v68, v68, v69
	v_cvt_pk_f16_f32 v69, v74, v75
	global_store_dwordx4 v[86:87], v[66:69], off offset:256
	s_nop 0
	v_lshl_add_u64 v[70:71], s[8:9], 0, v[78:79]
;     __device__ __forceinline__ void operator()(const Acc& acc, const Unit& u, int wr, int wc, int fr, int fq) const {
;     ...
;         for (int ai = 0; ai < 2; ++ai)
; #pragma unroll
;             for (int m = 0; m < 4; ++m) { const size_t off = (size_t)(u.pm * BM + ai * HALF + wr * 64 + m * 16 + fr) * DM + col0;
; #pragma unroll
;                 for (int bj = 0; bj < 2; ++bj) { f32x4 b0, b1;
;                     if constexpr (BASE16) { const f16x8 bv = *(const f16x8*)((const f16*)base + off + bj * HALF);
;                         b0 = (f32x4){(float)bv[0], (float)bv[1], (float)bv[2], (float)bv[3]}; b1 = (f32x4){(float)bv[4], (float)bv[5], (float)bv[6], (float)bv[7]}; }
;                     else { b0 = *(const f32x4*)((const float*)base + off + bj * HALF); b1 = *(const f32x4*)((const float*)base + off + bj * HALF + 4); }
;                     const f32x4 v0 = b0 + gv[bj][0] * acc[ai][bj][m][0], v1 = b1 + gv[bj][1] * acc[ai][bj][m][1];
;                     u32x4 w; w.x = pkh(v0[0], v0[1]); w.y = pkh(v0[2], v0[3]); w.z = pkh(v1[0], v1[1]); w.w = pkh(v1[2], v1[3]);
;                     *(u32x4*)(out + off + bj * HALF) = w; }
;                 if (m & 1) asm volatile("" ::: "memory"); }
	s_nop 0
	v_mov_b32_e32 v66, v214
	v_mov_b32_e32 v67, v215
	v_mov_b32_e32 v68, v216
	v_mov_b32_e32 v69, v217
	v_cvt_f32_f16_e32 v72, v66
	v_cvt_f32_f16_sdwa v73, v66 dst_sel:DWORD dst_unused:UNUSED_PAD src0_sel:WORD_1
	v_cvt_f32_f16_e32 v66, v67
	v_cvt_f32_f16_sdwa v67, v67 dst_sel:DWORD dst_unused:UNUSED_PAD src0_sel:WORD_1
	v_cvt_f32_f16_e32 v74, v68
	v_cvt_f32_f16_e32 v76, v69
	v_cvt_f32_f16_sdwa v77, v69 dst_sel:DWORD dst_unused:UNUSED_PAD src0_sel:WORD_1
	v_cvt_f32_f16_sdwa v75, v68 dst_sel:DWORD dst_unused:UNUSED_PAD src0_sel:WORD_1
	v_pk_fma_f32 v[64:65], v[64:65], v[128:129], v[66:67]
	v_pk_fma_f32 v[62:63], v[62:63], v[126:127], v[72:73]
	v_pk_fma_f32 v[66:67], v[60:61], v[124:125], v[76:77]
	v_pk_fma_f32 v[60:61], v[58:59], v[122:123], v[74:75]
	v_cvt_pk_f16_f32 v58, v62, v63
	v_cvt_pk_f16_f32 v59, v64, v65
	v_cvt_pk_f16_f32 v60, v60, v61
	v_cvt_pk_f16_f32 v61, v66, v67
	global_store_dwordx4 v[70:71], v[58:61], off
	s_nop 0
	v_add_u32_e32 v62, 0x90, v164
	v_ashrrev_i32_e32 v63, 31, v62
	v_lshlrev_b64 v[62:63], 10, v[62:63]
	v_lshl_add_u64 v[62:63], v[62:63], 0, v[162:163]
	v_lshlrev_b64 v[62:63], 1, v[62:63]
	v_lshl_add_u64 v[64:65], s[66:67], 0, v[62:63]
	s_nop 0
	v_mov_b32_e32 v58, v218
	v_mov_b32_e32 v59, v219
	v_mov_b32_e32 v60, v220
	v_mov_b32_e32 v61, v221
	v_cvt_f32_f16_e32 v66, v58
	v_cvt_f32_f16_sdwa v67, v58 dst_sel:DWORD dst_unused:UNUSED_PAD src0_sel:WORD_1
	v_cvt_f32_f16_e32 v58, v59
	v_cvt_f32_f16_sdwa v59, v59 dst_sel:DWORD dst_unused:UNUSED_PAD src0_sel:WORD_1
	v_cvt_f32_f16_e32 v68, v60
	v_cvt_f32_f16_e32 v72, v61
	v_cvt_f32_f16_sdwa v73, v61 dst_sel:DWORD dst_unused:UNUSED_PAD src0_sel:WORD_1
	v_cvt_f32_f16_sdwa v69, v60 dst_sel:DWORD dst_unused:UNUSED_PAD src0_sel:WORD_1
	v_pk_fma_f32 v[56:57], v[56:57], v[136:137], v[58:59]
	v_pk_fma_f32 v[54:55], v[54:55], v[134:135], v[66:67]
	v_pk_fma_f32 v[58:59], v[52:53], v[132:133], v[72:73]
	v_pk_fma_f32 v[52:53], v[50:51], v[130:131], v[68:69]
	v_cvt_pk_f16_f32 v50, v54, v55
	v_cvt_pk_f16_f32 v51, v56, v57
	v_cvt_pk_f16_f32 v52, v52, v53
	v_cvt_pk_f16_f32 v53, v58, v59
	global_store_dwordx4 v[70:71], v[50:53], off offset:256
	s_nop 0
	v_lshl_add_u64 v[54:55], s[8:9], 0, v[62:63]
	s_nop 0
	v_mov_b32_e32 v50, v222
	v_mov_b32_e32 v51, v223
	v_mov_b32_e32 v52, v224
	v_mov_b32_e32 v53, v225
	v_cvt_f32_f16_e32 v56, v50
	v_cvt_f32_f16_sdwa v57, v50 dst_sel:DWORD dst_unused:UNUSED_PAD src0_sel:WORD_1
	v_cvt_f32_f16_e32 v50, v51
	v_cvt_f32_f16_sdwa v51, v51 dst_sel:DWORD dst_unused:UNUSED_PAD src0_sel:WORD_1
	v_cvt_f32_f16_e32 v58, v52
	v_cvt_f32_f16_e32 v60, v53
	v_cvt_f32_f16_sdwa v61, v53 dst_sel:DWORD dst_unused:UNUSED_PAD src0_sel:WORD_1
	v_cvt_f32_f16_sdwa v59, v52 dst_sel:DWORD dst_unused:UNUSED_PAD src0_sel:WORD_1
	v_pk_fma_f32 v[48:49], v[48:49], v[128:129], v[50:51]
	v_pk_fma_f32 v[46:47], v[46:47], v[126:127], v[56:57]
	v_pk_fma_f32 v[50:51], v[44:45], v[124:125], v[60:61]
	v_pk_fma_f32 v[44:45], v[42:43], v[122:123], v[58:59]
	v_cvt_pk_f16_f32 v42, v46, v47
	v_cvt_pk_f16_f32 v43, v48, v49
	v_cvt_pk_f16_f32 v44, v44, v45
	v_cvt_pk_f16_f32 v45, v50, v51
	global_store_dwordx4 v[54:55], v[42:45], off
	s_nop 0
	v_add_u32_e32 v46, 0xa0, v164
	v_ashrrev_i32_e32 v47, 31, v46
	v_lshlrev_b64 v[46:47], 10, v[46:47]
	v_lshl_add_u64 v[46:47], v[46:47], 0, v[162:163]
	v_lshlrev_b64 v[46:47], 1, v[46:47]
	v_lshl_add_u64 v[48:49], s[66:67], 0, v[46:47]
	s_nop 0
	v_mov_b32_e32 v42, v226
	v_mov_b32_e32 v43, v227
	v_mov_b32_e32 v44, v228
	v_mov_b32_e32 v45, v229
	v_cvt_f32_f16_e32 v50, v42
	v_cvt_f32_f16_sdwa v51, v42 dst_sel:DWORD dst_unused:UNUSED_PAD src0_sel:WORD_1
	v_cvt_f32_f16_e32 v42, v43
	v_cvt_f32_f16_sdwa v43, v43 dst_sel:DWORD dst_unused:UNUSED_PAD src0_sel:WORD_1
	v_cvt_f32_f16_e32 v52, v44
	v_cvt_f32_f16_e32 v56, v45
	v_cvt_f32_f16_sdwa v57, v45 dst_sel:DWORD dst_unused:UNUSED_PAD src0_sel:WORD_1
	v_cvt_f32_f16_sdwa v53, v44 dst_sel:DWORD dst_unused:UNUSED_PAD src0_sel:WORD_1
	v_pk_fma_f32 v[40:41], v[40:41], v[136:137], v[42:43]
	v_pk_fma_f32 v[38:39], v[38:39], v[134:135], v[50:51]
	v_pk_fma_f32 v[42:43], v[36:37], v[132:133], v[56:57]
	v_pk_fma_f32 v[36:37], v[34:35], v[130:131], v[52:53]
	v_cvt_pk_f16_f32 v34, v38, v39
	v_cvt_pk_f16_f32 v35, v40, v41
	v_cvt_pk_f16_f32 v36, v36, v37
	v_cvt_pk_f16_f32 v37, v42, v43
;     __device__ __forceinline__ void operator()(const Acc& acc, const Unit& u, int wr, int wc, int fr, int fq) const {
;     ...
;         for (int ai = 0; ai < 2; ++ai)
; #pragma unroll
;             for (int m = 0; m < 4; ++m) { const size_t off = (size_t)(u.pm * BM + ai * HALF + wr * 64 + m * 16 + fr) * DM + col0;
; #pragma unroll
;                 for (int bj = 0; bj < 2; ++bj) { f32x4 b0, b1;
;                     if constexpr (BASE16) { const f16x8 bv = *(const f16x8*)((const f16*)base + off + bj * HALF);
;                         b0 = (f32x4){(float)bv[0], (float)bv[1], (float)bv[2], (float)bv[3]}; b1 = (f32x4){(float)bv[4], (float)bv[5], (float)bv[6], (float)bv[7]}; }
;                     else { b0 = *(const f32x4*)((const float*)base + off + bj * HALF); b1 = *(const f32x4*)((const float*)base + off + bj * HALF + 4); }
;                     const f32x4 v0 = b0 + gv[bj][0] * acc[ai][bj][m][0], v1 = b1 + gv[bj][1] * acc[ai][bj][m][1];
;                     u32x4 w; w.x = pkh(v0[0], v0[1]); w.y = pkh(v0[2], v0[3]); w.z = pkh(v1[0], v1[1]); w.w = pkh(v1[2], v1[3]);
;                     *(u32x4*)(out + off + bj * HALF) = w; }
;                 if (m & 1) asm volatile("" ::: "memory"); }
	global_store_dwordx4 v[54:55], v[34:37], off offset:256
	s_nop 0
	v_lshl_add_u64 v[38:39], s[8:9], 0, v[46:47]
	s_nop 0
	v_mov_b32_e32 v34, v230
	v_mov_b32_e32 v35, v231
	v_mov_b32_e32 v36, v232
	v_mov_b32_e32 v37, v233
	v_cvt_f32_f16_e32 v40, v34
	v_cvt_f32_f16_sdwa v41, v34 dst_sel:DWORD dst_unused:UNUSED_PAD src0_sel:WORD_1
	v_cvt_f32_f16_e32 v34, v35
	v_cvt_f32_f16_sdwa v35, v35 dst_sel:DWORD dst_unused:UNUSED_PAD src0_sel:WORD_1
	v_cvt_f32_f16_e32 v42, v36
	v_cvt_f32_f16_e32 v44, v37
	v_cvt_f32_f16_sdwa v45, v37 dst_sel:DWORD dst_unused:UNUSED_PAD src0_sel:WORD_1
	v_cvt_f32_f16_sdwa v43, v36 dst_sel:DWORD dst_unused:UNUSED_PAD src0_sel:WORD_1
	v_pk_fma_f32 v[32:33], v[32:33], v[128:129], v[34:35]
	v_pk_fma_f32 v[30:31], v[30:31], v[126:127], v[40:41]
	v_pk_fma_f32 v[34:35], v[28:29], v[124:125], v[44:45]
	v_pk_fma_f32 v[28:29], v[26:27], v[122:123], v[42:43]
	v_cvt_pk_f16_f32 v26, v30, v31
	v_cvt_pk_f16_f32 v27, v32, v33
	v_cvt_pk_f16_f32 v28, v28, v29
	v_cvt_pk_f16_f32 v29, v34, v35
	global_store_dwordx4 v[38:39], v[26:29], off
	s_nop 0
	v_add_u32_e32 v30, 0xb0, v164
	v_ashrrev_i32_e32 v31, 31, v30
	v_lshlrev_b64 v[30:31], 10, v[30:31]
	v_lshl_add_u64 v[30:31], v[30:31], 0, v[162:163]
	v_lshlrev_b64 v[30:31], 1, v[30:31]
	v_lshl_add_u64 v[32:33], s[66:67], 0, v[30:31]
	s_nop 0
	v_mov_b32_e32 v26, v234
	v_mov_b32_e32 v27, v235
	v_mov_b32_e32 v28, v236
	v_mov_b32_e32 v29, v237
	v_cvt_f32_f16_e32 v34, v26
	v_cvt_f32_f16_sdwa v35, v26 dst_sel:DWORD dst_unused:UNUSED_PAD src0_sel:WORD_1
	v_cvt_f32_f16_e32 v26, v27
	v_cvt_f32_f16_sdwa v27, v27 dst_sel:DWORD dst_unused:UNUSED_PAD src0_sel:WORD_1
	v_cvt_f32_f16_e32 v36, v28
	v_cvt_f32_f16_e32 v40, v29
	v_cvt_f32_f16_sdwa v41, v29 dst_sel:DWORD dst_unused:UNUSED_PAD src0_sel:WORD_1
	v_cvt_f32_f16_sdwa v37, v28 dst_sel:DWORD dst_unused:UNUSED_PAD src0_sel:WORD_1
	v_pk_fma_f32 v[24:25], v[24:25], v[136:137], v[26:27]
	v_pk_fma_f32 v[22:23], v[22:23], v[134:135], v[34:35]
	v_pk_fma_f32 v[26:27], v[20:21], v[132:133], v[40:41]
	v_pk_fma_f32 v[20:21], v[18:19], v[130:131], v[36:37]
	v_cvt_pk_f16_f32 v18, v22, v23
	v_cvt_pk_f16_f32 v19, v24, v25
	v_cvt_pk_f16_f32 v20, v20, v21
	v_cvt_pk_f16_f32 v21, v26, v27
	global_store_dwordx4 v[38:39], v[18:21], off offset:256
	s_nop 0
	v_lshl_add_u64 v[22:23], s[8:9], 0, v[30:31]
	s_nop 0
	v_mov_b32_e32 v18, v238
	v_mov_b32_e32 v19, v239
	v_mov_b32_e32 v20, v240
	v_mov_b32_e32 v21, v241
	v_cvt_f32_f16_e32 v24, v18
	v_cvt_f32_f16_sdwa v25, v18 dst_sel:DWORD dst_unused:UNUSED_PAD src0_sel:WORD_1
	v_cvt_f32_f16_e32 v18, v19
	v_cvt_f32_f16_sdwa v19, v19 dst_sel:DWORD dst_unused:UNUSED_PAD src0_sel:WORD_1
	v_cvt_f32_f16_e32 v26, v20
	v_cvt_f32_f16_e32 v28, v21
	v_cvt_f32_f16_sdwa v29, v21 dst_sel:DWORD dst_unused:UNUSED_PAD src0_sel:WORD_1
	v_cvt_f32_f16_sdwa v27, v20 dst_sel:DWORD dst_unused:UNUSED_PAD src0_sel:WORD_1
	v_pk_fma_f32 v[16:17], v[16:17], v[128:129], v[18:19]
	v_pk_fma_f32 v[14:15], v[14:15], v[126:127], v[24:25]
	v_pk_fma_f32 v[18:19], v[12:13], v[124:125], v[28:29]
	v_pk_fma_f32 v[12:13], v[10:11], v[122:123], v[26:27]
	v_cvt_pk_f16_f32 v10, v14, v15
	v_cvt_pk_f16_f32 v11, v16, v17
	v_cvt_pk_f16_f32 v12, v12, v13
	v_cvt_pk_f16_f32 v13, v18, v19
	global_store_dwordx4 v[22:23], v[10:13], off
	s_nop 0
	s_nop 0
	v_mov_b32_e32 v10, v242
	v_mov_b32_e32 v11, v243
	v_mov_b32_e32 v12, v244
	v_mov_b32_e32 v13, v245
	v_cvt_f32_f16_e32 v14, v10
	v_cvt_f32_f16_sdwa v15, v10 dst_sel:DWORD dst_unused:UNUSED_PAD src0_sel:WORD_1
	v_cvt_f32_f16_e32 v10, v11
	v_cvt_f32_f16_sdwa v11, v11 dst_sel:DWORD dst_unused:UNUSED_PAD src0_sel:WORD_1
	v_cvt_f32_f16_e32 v16, v12
	v_cvt_f32_f16_e32 v18, v13
	v_cvt_f32_f16_sdwa v19, v13 dst_sel:DWORD dst_unused:UNUSED_PAD src0_sel:WORD_1
	v_cvt_f32_f16_sdwa v17, v12 dst_sel:DWORD dst_unused:UNUSED_PAD src0_sel:WORD_1
	v_pk_fma_f32 v[8:9], v[8:9], v[136:137], v[10:11]
	v_pk_fma_f32 v[6:7], v[6:7], v[134:135], v[14:15]
	v_pk_fma_f32 v[10:11], v[4:5], v[132:133], v[18:19]
	v_pk_fma_f32 v[4:5], v[2:3], v[130:131], v[16:17]
	v_cvt_pk_f16_f32 v2, v6, v7
	v_cvt_pk_f16_f32 v3, v8, v9
	v_cvt_pk_f16_f32 v4, v4, v5
	v_cvt_pk_f16_f32 v5, v10, v11
	global_store_dwordx4 v[22:23], v[2:5], off offset:256
	s_cbranch_vccnz .LBB0_1472
	s_andn2_b64 vcc, exec, s[6:7]
	s_cbranch_vccnz .LBB0_1471
	s_barrier
	s_branch .LBB0_1471
